# P0: non-temporal (nt) hint on the streaming read-once f32 loads of x / mem in the bf16 conversion pass
# speedup vs baseline: 1.0315x; 1.0315x over previous
.LBB0_62:
	s_add_i32 s4, s18, 0x4000
	s_ashr_i32 s5, s4, 31
	s_cmpk_lt_i32 s4, 0x4000
	s_cselect_b64 s[16:17], -1, 0
	s_and_b64 s[0:1], s[16:17], exec
	s_cselect_b32 s15, s5, 0
	s_cselect_b32 s14, s4, s18
	s_cselect_b32 s4, s53, s55
	s_cselect_b32 s5, s52, s54
	s_lshl_b64 s[0:1], s[14:15], 12
	s_add_u32 s0, s5, s0
	s_addc_u32 s1, s4, s1
	global_load_dwordx4 v[78:81], v1, s[0:1] nt
	global_load_dwordx4 v[74:77], v1, s[0:1] offset:1024 nt
	global_load_dwordx4 v[70:73], v1, s[0:1] offset:2048 nt
	global_load_dwordx4 v[66:69], v1, s[0:1] offset:3072 nt
	s_add_i32 s29, s92, s18
	s_add_i32 s30, s29, 0x4000
	s_cmpk_lt_i32 s30, 0x4800
	s_cselect_b64 s[12:13], -1, 0
	s_cmpk_gt_i32 s30, 0x47ff
	s_cbranch_scc1 .LBB0_64
	s_ashr_i32 s0, s30, 31
	s_cmpk_lt_i32 s30, 0x4000
	s_cselect_b32 s1, s0, 0
	s_cselect_b32 s0, s30, s29
	s_cselect_b32 s4, s53, s55
	s_cselect_b32 s5, s52, s54
	s_lshl_b64 s[0:1], s[0:1], 12
	s_add_u32 s0, s5, s0
	s_addc_u32 s1, s4, s1
	global_load_dwordx4 v[62:65], v1, s[0:1] nt
	global_load_dwordx4 v[58:61], v1, s[0:1] offset:1024 nt
	global_load_dwordx4 v[54:57], v1, s[0:1] offset:2048 nt
	global_load_dwordx4 v[50:53], v1, s[0:1] offset:3072 nt
.LBB0_64:
	s_add_i32 s27, s20, s18
	s_add_i32 s28, s27, 0x4000
	s_cmpk_lt_i32 s28, 0x4800
	s_cselect_b64 s[10:11], -1, 0
	s_cmpk_gt_i32 s28, 0x47ff
	s_cbranch_scc1 .LBB0_66
	s_ashr_i32 s0, s28, 31
	s_cmpk_lt_i32 s28, 0x4000
	s_cselect_b32 s1, s0, 0
	s_cselect_b32 s0, s28, s27
	s_cselect_b32 s4, s53, s55
	s_cselect_b32 s5, s52, s54
	s_lshl_b64 s[0:1], s[0:1], 12
	s_add_u32 s0, s5, s0
	s_addc_u32 s1, s4, s1
	global_load_dwordx4 v[46:49], v1, s[0:1] nt
	global_load_dwordx4 v[42:45], v1, s[0:1] offset:1024 nt
	global_load_dwordx4 v[38:41], v1, s[0:1] offset:2048 nt
	global_load_dwordx4 v[34:37], v1, s[0:1] offset:3072 nt
.LBB0_66:
	s_add_i32 s25, s21, s18
	s_add_i32 s26, s25, 0x4000
	s_cmpk_lt_i32 s26, 0x4800
	s_cselect_b64 s[4:5], -1, 0
	s_cmpk_gt_i32 s26, 0x47ff
	s_cbranch_scc1 .LBB0_68
	s_ashr_i32 s0, s26, 31
	s_cmpk_lt_i32 s26, 0x4000
	s_cselect_b32 s1, s0, 0
	s_cselect_b32 s0, s26, s25
	s_cselect_b32 s23, s53, s55
	s_cselect_b32 s24, s52, s54
	s_lshl_b64 s[0:1], s[0:1], 12
	s_add_u32 s0, s24, s0
	s_addc_u32 s1, s23, s1
	global_load_dwordx4 v[30:33], v1, s[0:1] nt
	global_load_dwordx4 v[26:29], v1, s[0:1] offset:1024 nt
	global_load_dwordx4 v[22:25], v1, s[0:1] offset:2048 nt
	global_load_dwordx4 v[18:21], v1, s[0:1] offset:3072 nt
.LBB0_68:
	s_add_i32 s23, s22, s18
	s_add_i32 s24, s23, 0x4000
	s_cmpk_lt_i32 s24, 0x4800
	s_cselect_b64 s[0:1], -1, 0
	s_cmpk_gt_i32 s24, 0x47ff
	s_cbranch_scc1 .LBB0_70
	s_ashr_i32 s31, s24, 31
	s_cmpk_lt_i32 s24, 0x4000
	s_cselect_b32 s35, s31, 0
	s_cselect_b32 s34, s24, s23
	s_cselect_b32 s31, s53, s55
	s_cselect_b32 s36, s52, s54
	s_lshl_b64 s[34:35], s[34:35], 12
	s_add_u32 s34, s36, s34
	s_addc_u32 s35, s31, s35
	global_load_dwordx4 v[14:17], v1, s[34:35] nt
	global_load_dwordx4 v[10:13], v1, s[34:35] offset:1024 nt
	global_load_dwordx4 v[6:9], v1, s[34:35] offset:2048 nt
	global_load_dwordx4 v[2:5], v1, s[34:35] offset:3072 nt
